# out-projection phase: half of the workgroups (block index bit 3) start ~12 us late so their HBM-bound residual epilogues fall into the other half's K-loops
# baseline (speedup 1.0000x reference)
.LBB0_1057:
	s_andn2_b64 vcc, exec, s[0:1]
	s_cbranch_vccnz .LBB0_1194
	v_readlane_b32 s0, v254, 60
	s_bitcmp1_b32 s0, 3
	s_cbranch_scc0 .Lz1_go
	s_sleep 127
	s_sleep 127
	s_sleep 127
.Lz1_go:
	v_readlane_b32 s0, v253, 34
	s_waitcnt vmcnt(0)
	v_mov_b32_e32 v12, v0
	v_readlane_b32 s1, v253, 35
	s_andn2_b64 vcc, exec, s[0:1]
	v_readfirstlane_b32 s0, v12
	s_cbranch_vccnz .LBB0_1144
	v_lshlrev_b32_e32 v1, 4, v12
	v_add_u32_e32 v2, 0x2000, v1
	v_ashrrev_i32_e32 v3, 31, v2
	v_lshrrev_b32_e32 v3, 22, v3
	v_add_u32_e32 v3, v2, v3
	v_ashrrev_i32_e32 v6, 10, v3
	v_mul_i32_i24_e32 v3, 0x400, v6
	v_sub_u32_e32 v2, v2, v3
	v_lshrrev_b32_e32 v3, 4, v2
	v_bitop3_b32 v2, v3, v2, 32 bitop3:0x6c
	v_ashrrev_i32_e32 v3, 31, v2
	v_lshrrev_b32_e32 v3, 26, v3
	v_add_u32_e32 v3, v2, v3
	v_lshlrev_b32_e32 v4, 3, v6
	v_ashrrev_i32_e32 v7, 6, v3
	v_and_b32_e32 v4, -16, v4
	v_add_u32_e32 v4, v7, v4
	v_and_b32_e32 v5, 3, v7
	s_mov_b32 s12, 0x1fffe0
	v_lshrrev_b32_e32 v8, 2, v4
	v_lshlrev_b32_e32 v9, 1, v4
	v_and_b32_e32 v3, 0xc0, v3
	v_and_or_b32 v5, v4, s12, v5
	v_and_b32_e32 v8, 4, v8
	v_and_b32_e32 v9, 24, v9
	v_sub_u32_e32 v2, v2, v3
	v_or3_b32 v5, v5, v8, v9
	v_lshlrev_b32_e32 v8, 5, v6
	v_ashrrev_i16_sdwa v2, v226, sext(v2) dst_sel:DWORD dst_unused:UNUSED_PAD src0_sel:DWORD src1_sel:BYTE_0
	v_and_b32_e32 v9, 32, v8
	v_bfe_i32 v8, v2, 0, 16
	v_add_lshl_u32 v2, v9, v8, 1
	v_lshl_add_u32 v148, v5, 11, v2
	v_lshl_add_u32 v150, v4, 11, v2
	v_bfe_i32 v2, v12, 27, 1
	v_lshrrev_b32_e32 v2, 22, v2
	v_add_u32_e32 v2, v1, v2
	v_and_b32_e32 v2, 0xfffffc00, v2
	v_sub_u32_e32 v1, v1, v2
	v_lshrrev_b32_e32 v2, 4, v1
	v_ashrrev_i32_e32 v3, 31, v12
	v_bitop3_b32 v1, v2, v1, 32 bitop3:0x6c
	v_lshrrev_b32_e32 v3, 26, v3
	v_ashrrev_i32_e32 v2, 31, v1
	v_add_u32_e32 v3, v12, v3
	v_lshrrev_b32_e32 v2, 26, v2
	v_ashrrev_i32_e32 v10, 6, v3
	v_readlane_b32 s1, v254, 51
	v_add_u32_e32 v2, v1, v2
	v_lshlrev_b32_e32 v3, 3, v10
	s_bitcmp1_b32 s1, 0
	s_mov_b32 s1, 0x75e1000
	v_ashrrev_i32_e32 v9, 6, v2
	v_and_b32_e32 v3, -16, v3
	s_cselect_b32 s1, s1, 0xef1000
	v_add_u32_e32 v3, v9, v3
	s_add_u32 s2, s74, s1
	v_and_b32_e32 v4, 3, v9
	v_lshrrev_b32_e32 v5, 2, v3
	v_lshlrev_b32_e32 v11, 1, v3
	v_and_b32_e32 v2, 0xc0, v2
	s_addc_u32 s3, s75, 0
	s_ashr_i32 s1, s0, 6
	v_and_or_b32 v4, v3, s12, v4
	v_and_b32_e32 v5, 4, v5
	v_and_b32_e32 v11, 24, v11
	v_sub_u32_e32 v1, v1, v2
	s_ashr_i32 s38, s0, 8
	s_lshl_b32 s40, s1, 10
	v_or3_b32 v4, v4, v5, v11
	v_lshlrev_b32_e32 v5, 5, v10
	v_ashrrev_i16_sdwa v1, v226, sext(v1) dst_sel:DWORD dst_unused:UNUSED_PAD src0_sel:DWORD src1_sel:BYTE_0
	v_readlane_b32 s12, v253, 50
	v_and_b32_e32 v5, 32, v5
	v_bfe_i32 v11, v1, 0, 16
	v_readlane_b32 s13, v253, 51
	s_add_u32 s34, s2, s12
	v_add_lshl_u32 v1, v5, v11, 1
	s_addc_u32 s35, s3, s13
	s_add_i32 s41, s40, 0
	v_lshl_add_u32 v114, v4, 11, v1
	s_add_i32 m0, s41, 0x10000
	v_lshl_add_u32 v152, v3, 11, v1
	global_load_lds_dwordx4 v114, s[34:35]
	s_add_i32 m0, s41, 0x12000
	s_add_u32 s12, s34, 0x40000
	global_load_lds_dwordx4 v148, s[34:35]
	s_addc_u32 s13, s35, 0
	s_add_i32 m0, s41, 0x14000
	s_add_i32 s42, s41, 0x2000
	global_load_lds_dwordx4 v114, s[12:13]
	s_add_i32 m0, s41, 0x16000
	s_add_i32 s43, s41, 0x4000
	global_load_lds_dwordx4 v148, s[12:13]
	v_readlane_b32 s12, v253, 60
	s_mov_b32 m0, s41
	v_readlane_b32 s13, v253, 61
	s_add_i32 s44, s41, 0x6000
	v_mov_b32_e32 v149, v115
	s_cmp_eq_u32 s38, 1
	v_lshl_add_u64 v[2:3], s[34:35], 0, v[114:115]
	v_lshl_add_u64 v[4:5], s[34:35], 0, v[148:149]
	global_load_lds_dwordx4 v152, s[12:13]
	s_mov_b32 m0, s42
	s_nop 0
	global_load_lds_dwordx4 v150, s[12:13]
	v_readlane_b32 s12, v253, 62
	s_mov_b32 m0, s43
	v_readlane_b32 s13, v253, 63
	s_nop 4
	global_load_lds_dwordx4 v152, s[12:13]
	s_mov_b32 m0, s44
	s_nop 0
	global_load_lds_dwordx4 v150, s[12:13]
	s_cselect_b64 s[12:13], -1, 0
	s_cmp_lg_u32 s38, 1
	s_cbranch_scc1 .LBB0_1061
	s_barrier
